# gather counted waits: u-section loops limited to 6 rows in flight (vmcnt 5), v-section stays at 7
# speedup vs baseline: 1.0055x; 1.0015x over previous
.LBB0_1419:
	v_mov_b32_e32 v69, v1
	v_mov_b32_e32 v83, v1
	s_waitcnt vmcnt(5)
	v_dot8c_i32_i4_e32 v69, v6, v74
	v_dot8c_i32_i4_e32 v83, v6, v70
	v_dot8c_i32_i4_e32 v69, v7, v75
	v_dot8c_i32_i4_e32 v83, v7, v71
	s_add_i32 s62, s57, -15
	v_dot8c_i32_i4_e32 v69, v8, v76
	v_dot8c_i32_i4_e32 v83, v8, v72
	s_cmp_lt_u32 s56, 3
	v_dot8c_i32_i4_e32 v69, v9, v77
	v_dot8c_i32_i4_e32 v83, v9, v73
	s_cselect_b64 vcc, -1, 0
	s_nop 1
	v_lshl_add_u32 v6, v69, 4, v83
	v_cndmask_b32_e32 v83, v79, v78, vcc
	v_cvt_f32_i32_e32 v69, v6
	v_readlane_b32 s62, v83, s62
	s_lshl_b32 s62, s62, 10
	s_nop 3
	buffer_load_dwordx4 v[6:9], v0, s[92:95], s62 offen
	v_mov_b32_e32 v84, v1
	v_mov_b32_e32 v85, v1
	s_waitcnt vmcnt(5)
	v_dot8c_i32_i4_e32 v84, v14, v74
	v_dot8c_i32_i4_e32 v85, v14, v70
	v_dot8c_i32_i4_e32 v84, v15, v75
	v_dot8c_i32_i4_e32 v85, v15, v71
	v_dot8c_i32_i4_e32 v84, v16, v76
	v_dot8c_i32_i4_e32 v85, v16, v72
	s_add_i32 s62, s57, -14
	v_dot8c_i32_i4_e32 v84, v17, v77
	v_dot8c_i32_i4_e32 v85, v17, v73
	v_readlane_b32 s62, v83, s62
	s_lshl_b32 s62, s62, 10
	s_nop 0
	v_lshl_add_u32 v14, v84, 4, v85
	v_cvt_f32_i32_e32 v84, v14
	s_nop 0
	buffer_load_dwordx4 v[14:17], v0, s[92:95], s62 offen
	v_mov_b32_e32 v85, v1
	v_mov_b32_e32 v86, v1
	s_waitcnt vmcnt(5)
	v_dot8c_i32_i4_e32 v85, v30, v74
	v_dot8c_i32_i4_e32 v86, v30, v70
	v_dot8c_i32_i4_e32 v85, v31, v75
	v_dot8c_i32_i4_e32 v86, v31, v71
	v_dot8c_i32_i4_e32 v85, v32, v76
	v_dot8c_i32_i4_e32 v86, v32, v72
	s_add_i32 s62, s57, -13
	v_dot8c_i32_i4_e32 v85, v33, v77
	v_dot8c_i32_i4_e32 v86, v33, v73
	v_readlane_b32 s62, v83, s62
	s_lshl_b32 s62, s62, 10
	s_nop 0
	v_lshl_add_u32 v30, v85, 4, v86
	v_cvt_f32_i32_e32 v85, v30
	s_nop 0
	buffer_load_dwordx4 v[30:33], v0, s[92:95], s62 offen
	v_mov_b32_e32 v86, v1
	v_mov_b32_e32 v87, v1
	s_waitcnt vmcnt(5)
	v_dot8c_i32_i4_e32 v86, v46, v74
	v_dot8c_i32_i4_e32 v87, v46, v70
	v_dot8c_i32_i4_e32 v86, v47, v75
	v_dot8c_i32_i4_e32 v87, v47, v71
	v_dot8c_i32_i4_e32 v86, v48, v76
	v_dot8c_i32_i4_e32 v87, v48, v72
	s_add_i32 s62, s57, -12
	v_dot8c_i32_i4_e32 v86, v49, v77
	v_dot8c_i32_i4_e32 v87, v49, v73
	v_readlane_b32 s62, v83, s62
	s_lshl_b32 s62, s62, 10
	s_nop 0
	v_lshl_add_u32 v46, v86, 4, v87
	v_cvt_f32_i32_e32 v86, v46
	s_nop 0
	buffer_load_dwordx4 v[46:49], v0, s[92:95], s62 offen
	v_mov_b32_e32 v87, v1
	v_mov_b32_e32 v88, v1
	s_waitcnt vmcnt(5)
	v_dot8c_i32_i4_e32 v87, v2, v74
	v_dot8c_i32_i4_e32 v88, v2, v70
	v_dot8c_i32_i4_e32 v87, v3, v75
	v_dot8c_i32_i4_e32 v88, v3, v71
	v_dot8c_i32_i4_e32 v87, v4, v76
	v_dot8c_i32_i4_e32 v88, v4, v72
	s_add_i32 s62, s57, -11
	v_dot8c_i32_i4_e32 v87, v5, v77
	v_dot8c_i32_i4_e32 v88, v5, v73
	v_readlane_b32 s62, v83, s62
	s_lshl_b32 s62, s62, 10
	s_nop 0
	v_lshl_add_u32 v2, v87, 4, v88
	v_cvt_f32_i32_e32 v87, v2
	s_nop 0
	buffer_load_dwordx4 v[2:5], v0, s[92:95], s62 offen
	v_mov_b32_e32 v88, v1
	v_mov_b32_e32 v89, v1
	s_waitcnt vmcnt(5)
	v_dot8c_i32_i4_e32 v88, v22, v74
	v_dot8c_i32_i4_e32 v89, v22, v70
	v_dot8c_i32_i4_e32 v88, v23, v75
	v_dot8c_i32_i4_e32 v89, v23, v71
	v_dot8c_i32_i4_e32 v88, v24, v76
	v_dot8c_i32_i4_e32 v89, v24, v72
	s_add_i32 s62, s57, -10
	v_dot8c_i32_i4_e32 v88, v25, v77
	v_dot8c_i32_i4_e32 v89, v25, v73
	v_readlane_b32 s62, v83, s62
	s_lshl_b32 s62, s62, 10
	s_nop 0
	v_lshl_add_u32 v22, v88, 4, v89
	v_cvt_f32_i32_e32 v88, v22
	s_nop 0
	buffer_load_dwordx4 v[22:25], v0, s[92:95], s62 offen
	v_mov_b32_e32 v89, v1
	v_mov_b32_e32 v90, v1
	s_waitcnt vmcnt(5)
	v_dot8c_i32_i4_e32 v89, v38, v74
	v_dot8c_i32_i4_e32 v90, v38, v70
	v_dot8c_i32_i4_e32 v89, v39, v75
	v_dot8c_i32_i4_e32 v90, v39, v71
	v_dot8c_i32_i4_e32 v89, v40, v76
	v_dot8c_i32_i4_e32 v90, v40, v72
	s_add_i32 s62, s57, -9
	v_dot8c_i32_i4_e32 v89, v41, v77
	v_dot8c_i32_i4_e32 v90, v41, v73
	v_readlane_b32 s62, v83, s62
	s_lshl_b32 s62, s62, 10
	s_nop 0
	v_lshl_add_u32 v38, v89, 4, v90
	v_cvt_f32_i32_e32 v89, v38
	s_nop 0
	buffer_load_dwordx4 v[38:41], v0, s[92:95], s62 offen
	v_mov_b32_e32 v90, v1
	v_mov_b32_e32 v91, v1
	s_waitcnt vmcnt(5)
	v_dot8c_i32_i4_e32 v90, v54, v74
	v_dot8c_i32_i4_e32 v91, v54, v70
	v_dot8c_i32_i4_e32 v90, v55, v75
	v_dot8c_i32_i4_e32 v91, v55, v71
	v_dot8c_i32_i4_e32 v90, v56, v76
	v_dot8c_i32_i4_e32 v91, v56, v72
	s_add_i32 s62, s57, -8
	v_dot8c_i32_i4_e32 v90, v57, v77
	v_dot8c_i32_i4_e32 v91, v57, v73
	v_readlane_b32 s62, v83, s62
	s_lshl_b32 s62, s62, 10
	s_nop 0
	v_lshl_add_u32 v54, v90, 4, v91
	v_cvt_f32_i32_e32 v90, v54
	s_nop 0
	buffer_load_dwordx4 v[54:57], v0, s[92:95], s62 offen
	v_mov_b32_e32 v91, v1
	v_mov_b32_e32 v92, v1
	s_waitcnt vmcnt(5)
	v_dot8c_i32_i4_e32 v91, v10, v74
	v_dot8c_i32_i4_e32 v92, v10, v70
	v_dot8c_i32_i4_e32 v91, v11, v75
	v_dot8c_i32_i4_e32 v92, v11, v71
	v_dot8c_i32_i4_e32 v91, v12, v76
	v_dot8c_i32_i4_e32 v92, v12, v72
	s_add_i32 s62, s57, -7
	v_dot8c_i32_i4_e32 v91, v13, v77
	v_dot8c_i32_i4_e32 v92, v13, v73
	v_readlane_b32 s62, v83, s62
	s_lshl_b32 s62, s62, 10
	s_nop 0
	v_lshl_add_u32 v10, v91, 4, v92
	v_cvt_f32_i32_e32 v91, v10
	s_nop 0
	buffer_load_dwordx4 v[10:13], v0, s[92:95], s62 offen
	v_mov_b32_e32 v92, v1
	v_mov_b32_e32 v93, v1
	s_waitcnt vmcnt(5)
	v_dot8c_i32_i4_e32 v92, v26, v74
	v_dot8c_i32_i4_e32 v93, v26, v70
	v_dot8c_i32_i4_e32 v92, v27, v75
	v_dot8c_i32_i4_e32 v93, v27, v71
	v_dot8c_i32_i4_e32 v92, v28, v76
	v_dot8c_i32_i4_e32 v93, v28, v72
	s_add_i32 s62, s57, -6
	v_dot8c_i32_i4_e32 v92, v29, v77
	v_dot8c_i32_i4_e32 v93, v29, v73
	v_readlane_b32 s62, v83, s62
	s_lshl_b32 s62, s62, 10
	s_nop 0
	v_lshl_add_u32 v26, v92, 4, v93
	v_cvt_f32_i32_e32 v92, v26
	s_nop 0
	buffer_load_dwordx4 v[26:29], v0, s[92:95], s62 offen
	v_mov_b32_e32 v93, v1
	v_mov_b32_e32 v94, v1
	s_waitcnt vmcnt(5)
	v_dot8c_i32_i4_e32 v93, v42, v74
	v_dot8c_i32_i4_e32 v94, v42, v70
	v_dot8c_i32_i4_e32 v93, v43, v75
	v_dot8c_i32_i4_e32 v94, v43, v71
	v_dot8c_i32_i4_e32 v93, v44, v76
	v_dot8c_i32_i4_e32 v94, v44, v72
	s_add_i32 s62, s57, -5
	v_dot8c_i32_i4_e32 v93, v45, v77
	v_dot8c_i32_i4_e32 v94, v45, v73
	v_readlane_b32 s62, v83, s62
	s_lshl_b32 s62, s62, 10
	s_nop 0
	v_lshl_add_u32 v42, v93, 4, v94
	v_cvt_f32_i32_e32 v93, v42
	s_nop 0
	buffer_load_dwordx4 v[42:45], v0, s[92:95], s62 offen
	v_mov_b32_e32 v94, v1
	v_mov_b32_e32 v95, v1
	s_waitcnt vmcnt(5)
	v_dot8c_i32_i4_e32 v94, v58, v74
	v_dot8c_i32_i4_e32 v95, v58, v70
	v_dot8c_i32_i4_e32 v94, v59, v75
	v_dot8c_i32_i4_e32 v95, v59, v71
	v_dot8c_i32_i4_e32 v94, v60, v76
	v_dot8c_i32_i4_e32 v95, v60, v72
	s_add_i32 s62, s57, -4
	v_dot8c_i32_i4_e32 v94, v61, v77
	v_dot8c_i32_i4_e32 v95, v61, v73
	v_readlane_b32 s62, v83, s62
	s_lshl_b32 s62, s62, 10
	s_nop 0
	v_lshl_add_u32 v58, v94, 4, v95
	v_cvt_f32_i32_e32 v94, v58
	s_nop 0
	buffer_load_dwordx4 v[58:61], v0, s[92:95], s62 offen
	v_mov_b32_e32 v95, v1
	v_mov_b32_e32 v96, v1
	s_waitcnt vmcnt(5)
	v_dot8c_i32_i4_e32 v95, v18, v74
	v_dot8c_i32_i4_e32 v96, v18, v70
	v_dot8c_i32_i4_e32 v95, v19, v75
	v_dot8c_i32_i4_e32 v96, v19, v71
	v_dot8c_i32_i4_e32 v95, v20, v76
	v_dot8c_i32_i4_e32 v96, v20, v72
	s_add_i32 s62, s57, -3
	v_dot8c_i32_i4_e32 v95, v21, v77
	v_dot8c_i32_i4_e32 v96, v21, v73
	v_readlane_b32 s62, v83, s62
	s_lshl_b32 s62, s62, 10
	s_nop 0
	v_lshl_add_u32 v18, v95, 4, v96
	v_cvt_f32_i32_e32 v95, v18
	s_nop 0
	buffer_load_dwordx4 v[18:21], v0, s[92:95], s62 offen
	v_mov_b32_e32 v96, v1
	v_mov_b32_e32 v97, v1
	s_waitcnt vmcnt(5)
	v_dot8c_i32_i4_e32 v96, v34, v74
	v_dot8c_i32_i4_e32 v97, v34, v70
	v_dot8c_i32_i4_e32 v96, v35, v75
	v_dot8c_i32_i4_e32 v97, v35, v71
	v_dot8c_i32_i4_e32 v96, v36, v76
	v_dot8c_i32_i4_e32 v97, v36, v72
	s_add_i32 s62, s57, -2
	v_dot8c_i32_i4_e32 v96, v37, v77
	v_dot8c_i32_i4_e32 v97, v37, v73
	v_readlane_b32 s62, v83, s62
	s_lshl_b32 s62, s62, 10
	s_nop 0
	v_lshl_add_u32 v34, v96, 4, v97
	v_cvt_f32_i32_e32 v96, v34
	s_nop 0
	buffer_load_dwordx4 v[34:37], v0, s[92:95], s62 offen
	v_mov_b32_e32 v97, v1
	v_mov_b32_e32 v98, v1
	s_waitcnt vmcnt(5)
	v_dot8c_i32_i4_e32 v97, v50, v74
	v_dot8c_i32_i4_e32 v98, v50, v70
	v_dot8c_i32_i4_e32 v97, v51, v75
	v_dot8c_i32_i4_e32 v98, v51, v71
	v_dot8c_i32_i4_e32 v97, v52, v76
	v_dot8c_i32_i4_e32 v98, v52, v72
	s_add_i32 s62, s57, -1
	v_dot8c_i32_i4_e32 v97, v53, v77
	v_dot8c_i32_i4_e32 v98, v53, v73
	v_readlane_b32 s62, v83, s62
	s_lshl_b32 s62, s62, 10
	s_nop 0
	v_lshl_add_u32 v50, v97, 4, v98
	v_cvt_f32_i32_e32 v97, v50
	s_nop 0
	buffer_load_dwordx4 v[50:53], v0, s[92:95], s62 offen
	v_mov_b32_e32 v98, v1
	v_mov_b32_e32 v99, v1
	s_waitcnt vmcnt(5)
	v_dot8c_i32_i4_e32 v98, v62, v74
	v_dot8c_i32_i4_e32 v99, v62, v70
	v_dot8c_i32_i4_e32 v98, v63, v75
	v_dot8c_i32_i4_e32 v99, v63, v71
	v_readlane_b32 s62, v83, s57
	v_dot8c_i32_i4_e32 v98, v64, v76
	v_dot8c_i32_i4_e32 v99, v64, v72
	s_lshl_b32 s62, s62, 10
	v_dot8c_i32_i4_e32 v98, v65, v77
	v_dot8c_i32_i4_e32 v99, v65, v73
	buffer_load_dwordx4 v[62:65], v0, s[92:95], s62 offen
	s_nop 1
	v_lshl_add_u32 v83, v98, 4, v99
	v_cvt_f32_i32_e32 v83, v83
	v_cndmask_b32_e64 v98, v91, v69, s[0:1]
	v_cndmask_b32_e64 v69, v69, v91, s[0:1]
	v_cndmask_b32_e64 v91, v92, v84, s[0:1]
	v_cndmask_b32_e64 v84, v84, v92, s[0:1]
	v_cndmask_b32_e64 v92, v93, v85, s[0:1]
	v_cndmask_b32_e64 v85, v85, v93, s[0:1]
	v_cndmask_b32_e64 v93, v94, v86, s[0:1]
	v_cndmask_b32_e64 v86, v86, v94, s[0:1]
	v_cndmask_b32_e64 v94, v95, v87, s[0:1]
	v_cndmask_b32_e64 v87, v87, v95, s[0:1]
	v_cndmask_b32_e64 v95, v96, v88, s[0:1]
	v_cndmask_b32_e64 v88, v88, v96, s[0:1]
	v_cndmask_b32_e64 v96, v97, v89, s[0:1]
	v_cndmask_b32_e64 v89, v89, v97, s[0:1]
	v_cndmask_b32_e64 v97, v83, v90, s[0:1]
	v_cndmask_b32_e64 v83, v90, v83, s[0:1]
	ds_bpermute_b32 v69, v190, v69
	ds_bpermute_b32 v84, v190, v84
	ds_bpermute_b32 v85, v190, v85
	ds_bpermute_b32 v86, v190, v86
	ds_bpermute_b32 v87, v190, v87
	ds_bpermute_b32 v88, v190, v88
	ds_bpermute_b32 v89, v190, v89
	ds_bpermute_b32 v83, v190, v83
	s_waitcnt lgkmcnt(7)
	v_add_f32_e32 v69, v98, v69
	s_waitcnt lgkmcnt(6)
	v_add_f32_e32 v84, v91, v84
	s_waitcnt lgkmcnt(5)
	v_add_f32_e32 v85, v92, v85
	s_waitcnt lgkmcnt(4)
	v_add_f32_e32 v86, v93, v86
	s_waitcnt lgkmcnt(3)
	v_add_f32_e32 v87, v94, v87
	s_waitcnt lgkmcnt(2)
	v_add_f32_e32 v88, v95, v88
	s_waitcnt lgkmcnt(1)
	v_add_f32_e32 v89, v96, v89
	s_waitcnt lgkmcnt(0)
	v_add_f32_e32 v83, v97, v83
	v_cndmask_b32_e64 v90, v87, v69, s[2:3]
	v_cndmask_b32_e64 v69, v69, v87, s[2:3]
	v_cndmask_b32_e64 v87, v88, v84, s[2:3]
	v_cndmask_b32_e64 v84, v84, v88, s[2:3]
	v_cndmask_b32_e64 v88, v89, v85, s[2:3]
	v_cndmask_b32_e64 v85, v85, v89, s[2:3]
	v_cndmask_b32_e64 v89, v83, v86, s[2:3]
	v_cndmask_b32_e64 v83, v86, v83, s[2:3]
	ds_bpermute_b32 v69, v189, v69
	ds_bpermute_b32 v84, v189, v84
	ds_bpermute_b32 v85, v189, v85
	ds_bpermute_b32 v83, v189, v83
	s_add_i32 s57, s57, 16
	s_waitcnt lgkmcnt(3)
	v_add_f32_e32 v69, v90, v69
	s_waitcnt lgkmcnt(2)
	v_add_f32_e32 v84, v87, v84
	s_waitcnt lgkmcnt(1)
	v_add_f32_e32 v85, v88, v85
	s_waitcnt lgkmcnt(0)
	v_add_f32_e32 v83, v89, v83
	v_cndmask_b32_e64 v86, v85, v69, s[4:5]
	v_cndmask_b32_e64 v69, v69, v85, s[4:5]
	v_cndmask_b32_e64 v85, v83, v84, s[4:5]
	v_cndmask_b32_e64 v83, v84, v83, s[4:5]
	ds_bpermute_b32 v69, v188, v69
	ds_bpermute_b32 v83, v188, v83
	s_waitcnt lgkmcnt(1)
	v_add_f32_e32 v69, v86, v69
	s_waitcnt lgkmcnt(0)
	v_add_f32_e32 v83, v85, v83
	v_cndmask_b32_e64 v84, v83, v69, s[6:7]
	v_cndmask_b32_e64 v69, v69, v83, s[6:7]
	ds_bpermute_b32 v69, v163, v69
	s_waitcnt lgkmcnt(0)
	v_add_f32_e32 v69, v84, v69
	v_mov_b32_e32 v83, v69
	s_nop 1
	v_permlane16_swap_b32_e32 v69, v83
	v_add_f32_e32 v69, v69, v83
	v_mov_b32_e32 v83, v69
	s_nop 1
	v_permlane32_swap_b32_e32 v69, v83
	v_add_f32_e32 v69, v69, v83
	v_mul_f32_e32 v69, v66, v69
	v_fma_f32 v83, |v69|, s66, 1.0
	v_rcp_f32_e32 v83, v83
	v_mul_f32_e32 v84, v69, v69
	v_mul_f32_e32 v84, 0xbf38aa3b, v84
	v_exp_f32_e32 v84, v84
	v_fmamk_f32 v85, v83, 0x3f07dc22, v207
	v_fmaak_f32 v85, v83, v85, 0x3f35f0e3
	v_fmaak_f32 v85, v83, v85, 0xbe11a98e
	v_fmaak_f32 v85, v83, v85, 0x3e027906
	v_mul_f32_e32 v83, v83, v85
	v_mul_f32_e32 v83, v84, v83
	v_mul_f32_e32 v84, v69, v83
	v_fma_f32 v83, -v69, v83, v69
	v_cmp_gt_f32_e32 vcc, 0, v69
	s_nop 1
	v_cndmask_b32_e32 v69, v83, v84, vcc
	v_mul_f32_e32 v69, 0x3d4ccccd, v69
	v_mul_f32_e32 v69, v82, v69
	v_cmp_eq_u32_e32 vcc, s56, v193
	s_add_i32 s56, s56, 1
	s_cmpk_eq_i32 s57, 0x5f
	v_cndmask_b32_e32 v81, v81, v69, vcc
	s_cbranch_scc0 .LBB0_1419
	s_mov_b32 s56, 0
	v_mov_b32_e32 v82, 0
	s_movk_i32 s57, 0x5f
	s_cmp_eq_u32 s101, 0
	s_cbranch_scc1 .Lnb_1421
	s_barrier
.Lnb_1421:
.LBB0_1421:
	v_mov_b32_e32 v69, v1
	v_mov_b32_e32 v83, v1
	s_waitcnt vmcnt(5)
	v_dot8c_i32_i4_e32 v69, v6, v74
	v_dot8c_i32_i4_e32 v83, v6, v70
	v_dot8c_i32_i4_e32 v69, v7, v75
	v_dot8c_i32_i4_e32 v83, v7, v71
	v_dot8c_i32_i4_e32 v69, v8, v76
	v_dot8c_i32_i4_e32 v83, v8, v72
	s_add_i32 s62, s57, -15
	v_dot8c_i32_i4_e32 v69, v9, v77
	v_dot8c_i32_i4_e32 v83, v9, v73
	s_bitcmp0_b32 s62, 6
	s_cselect_b64 vcc, -1, 0
	s_nop 0
	v_lshl_add_u32 v6, v69, 4, v83
	v_cvt_f32_i32_e32 v69, v6
	v_cndmask_b32_e32 v6, v79, v78, vcc
	s_nop 0
	v_readlane_b32 s62, v6, s62
	s_lshl_b32 s63, s62, 10
	s_cmp_gt_u32 s56, 2
	s_cselect_b32 s62, 0x1000000, 0
	s_add_i32 s63, s63, s62
	buffer_load_dwordx4 v[6:9], v0, s[92:95], s63 offen
	v_mov_b32_e32 v83, v1
	v_mov_b32_e32 v84, v1
	s_waitcnt vmcnt(5)
	v_dot8c_i32_i4_e32 v83, v14, v74
	v_dot8c_i32_i4_e32 v84, v14, v70
	v_dot8c_i32_i4_e32 v83, v15, v75
	v_dot8c_i32_i4_e32 v84, v15, v71
	v_dot8c_i32_i4_e32 v83, v16, v76
	v_dot8c_i32_i4_e32 v84, v16, v72
	s_add_i32 s63, s57, -14
	v_dot8c_i32_i4_e32 v83, v17, v77
	v_dot8c_i32_i4_e32 v84, v17, v73
	s_bitcmp0_b32 s63, 6
	s_cselect_b64 vcc, -1, 0
	s_nop 0
	v_lshl_add_u32 v14, v83, 4, v84
	v_cvt_f32_i32_e32 v83, v14
	v_cndmask_b32_e32 v14, v79, v78, vcc
	s_nop 0
	v_readlane_b32 s63, v14, s63
	s_lshl_b32 s63, s63, 10
	s_add_i32 s63, s63, s62
	s_nop 2
	buffer_load_dwordx4 v[14:17], v0, s[92:95], s63 offen
	v_mov_b32_e32 v84, v1
	v_mov_b32_e32 v85, v1
	s_waitcnt vmcnt(5)
	v_dot8c_i32_i4_e32 v84, v30, v74
	v_dot8c_i32_i4_e32 v85, v30, v70
	v_dot8c_i32_i4_e32 v84, v31, v75
	v_dot8c_i32_i4_e32 v85, v31, v71
	v_dot8c_i32_i4_e32 v84, v32, v76
	v_dot8c_i32_i4_e32 v85, v32, v72
	s_add_i32 s63, s57, -13
	v_dot8c_i32_i4_e32 v84, v33, v77
	v_dot8c_i32_i4_e32 v85, v33, v73
	s_bitcmp0_b32 s63, 6
	s_cselect_b64 vcc, -1, 0
	s_nop 0
	v_lshl_add_u32 v30, v84, 4, v85
	v_cvt_f32_i32_e32 v84, v30
	v_cndmask_b32_e32 v30, v79, v78, vcc
	s_nop 0
	v_readlane_b32 s63, v30, s63
	s_lshl_b32 s63, s63, 10
	s_add_i32 s63, s63, s62
	s_nop 2
	buffer_load_dwordx4 v[30:33], v0, s[92:95], s63 offen
	v_mov_b32_e32 v85, v1
	v_mov_b32_e32 v86, v1
	s_waitcnt vmcnt(5)
	v_dot8c_i32_i4_e32 v85, v46, v74
	v_dot8c_i32_i4_e32 v86, v46, v70
	v_dot8c_i32_i4_e32 v85, v47, v75
	v_dot8c_i32_i4_e32 v86, v47, v71
	v_dot8c_i32_i4_e32 v85, v48, v76
	v_dot8c_i32_i4_e32 v86, v48, v72
	s_add_i32 s63, s57, -12
	v_dot8c_i32_i4_e32 v85, v49, v77
	v_dot8c_i32_i4_e32 v86, v49, v73
	s_bitcmp0_b32 s63, 6
	s_cselect_b64 vcc, -1, 0
	s_nop 0
	v_lshl_add_u32 v46, v85, 4, v86
	v_cvt_f32_i32_e32 v85, v46
	v_cndmask_b32_e32 v46, v79, v78, vcc
	s_nop 0
	v_readlane_b32 s63, v46, s63
	s_lshl_b32 s63, s63, 10
	s_add_i32 s63, s63, s62
	s_nop 2
	buffer_load_dwordx4 v[46:49], v0, s[92:95], s63 offen
	v_mov_b32_e32 v86, v1
	v_mov_b32_e32 v87, v1
	s_waitcnt vmcnt(5)
	v_dot8c_i32_i4_e32 v86, v2, v74
	v_dot8c_i32_i4_e32 v87, v2, v70
	v_dot8c_i32_i4_e32 v86, v3, v75
	v_dot8c_i32_i4_e32 v87, v3, v71
	v_dot8c_i32_i4_e32 v86, v4, v76
	v_dot8c_i32_i4_e32 v87, v4, v72
	s_add_i32 s63, s57, -11
	v_dot8c_i32_i4_e32 v86, v5, v77
	v_dot8c_i32_i4_e32 v87, v5, v73
	s_bitcmp0_b32 s63, 6
	s_cselect_b64 vcc, -1, 0
	s_nop 0
	v_lshl_add_u32 v2, v86, 4, v87
	v_cvt_f32_i32_e32 v86, v2
	v_cndmask_b32_e32 v2, v79, v78, vcc
	s_nop 0
	v_readlane_b32 s63, v2, s63
	s_lshl_b32 s63, s63, 10
	s_add_i32 s63, s63, s62
	s_nop 2
	buffer_load_dwordx4 v[2:5], v0, s[92:95], s63 offen
	v_mov_b32_e32 v87, v1
	v_mov_b32_e32 v88, v1
	s_waitcnt vmcnt(5)
	v_dot8c_i32_i4_e32 v87, v22, v74
	v_dot8c_i32_i4_e32 v88, v22, v70
	v_dot8c_i32_i4_e32 v87, v23, v75
	v_dot8c_i32_i4_e32 v88, v23, v71
	v_dot8c_i32_i4_e32 v87, v24, v76
	v_dot8c_i32_i4_e32 v88, v24, v72
	s_add_i32 s63, s57, -10
	v_dot8c_i32_i4_e32 v87, v25, v77
	v_dot8c_i32_i4_e32 v88, v25, v73
	s_bitcmp0_b32 s63, 6
	s_cselect_b64 vcc, -1, 0
	s_nop 0
	v_lshl_add_u32 v22, v87, 4, v88
	v_cvt_f32_i32_e32 v87, v22
	v_cndmask_b32_e32 v22, v79, v78, vcc
	s_nop 0
	v_readlane_b32 s63, v22, s63
	s_lshl_b32 s63, s63, 10
	s_add_i32 s63, s63, s62
	s_nop 2
	buffer_load_dwordx4 v[22:25], v0, s[92:95], s63 offen
	v_mov_b32_e32 v88, v1
	v_mov_b32_e32 v89, v1
	s_waitcnt vmcnt(5)
	v_dot8c_i32_i4_e32 v88, v38, v74
	v_dot8c_i32_i4_e32 v89, v38, v70
	v_dot8c_i32_i4_e32 v88, v39, v75
	v_dot8c_i32_i4_e32 v89, v39, v71
	v_dot8c_i32_i4_e32 v88, v40, v76
	v_dot8c_i32_i4_e32 v89, v40, v72
	s_add_i32 s63, s57, -9
	v_dot8c_i32_i4_e32 v88, v41, v77
	v_dot8c_i32_i4_e32 v89, v41, v73
	s_bitcmp0_b32 s63, 6
	s_cselect_b64 vcc, -1, 0
	s_nop 0
	v_lshl_add_u32 v38, v88, 4, v89
	v_cvt_f32_i32_e32 v88, v38
	v_cndmask_b32_e32 v38, v79, v78, vcc
	s_nop 0
	v_readlane_b32 s63, v38, s63
	s_lshl_b32 s63, s63, 10
	s_add_i32 s63, s63, s62
	s_nop 2
	buffer_load_dwordx4 v[38:41], v0, s[92:95], s63 offen
	v_mov_b32_e32 v89, v1
	v_mov_b32_e32 v90, v1
	s_waitcnt vmcnt(5)
	v_dot8c_i32_i4_e32 v89, v54, v74
	v_dot8c_i32_i4_e32 v90, v54, v70
	v_dot8c_i32_i4_e32 v89, v55, v75
	v_dot8c_i32_i4_e32 v90, v55, v71
	v_dot8c_i32_i4_e32 v89, v56, v76
	v_dot8c_i32_i4_e32 v90, v56, v72
	s_add_i32 s63, s57, -8
	v_dot8c_i32_i4_e32 v89, v57, v77
	v_dot8c_i32_i4_e32 v90, v57, v73
	s_bitcmp0_b32 s63, 6
	s_cselect_b64 vcc, -1, 0
	s_nop 0
	v_lshl_add_u32 v54, v89, 4, v90
	v_cvt_f32_i32_e32 v89, v54
	v_cndmask_b32_e32 v54, v79, v78, vcc
	s_nop 0
	v_readlane_b32 s63, v54, s63
	s_lshl_b32 s63, s63, 10
	s_add_i32 s63, s63, s62
	s_nop 2
	buffer_load_dwordx4 v[54:57], v0, s[92:95], s63 offen
	v_mov_b32_e32 v90, v1
	v_mov_b32_e32 v91, v1
	s_waitcnt vmcnt(5)
	v_dot8c_i32_i4_e32 v90, v10, v74
	v_dot8c_i32_i4_e32 v91, v10, v70
	v_dot8c_i32_i4_e32 v90, v11, v75
	v_dot8c_i32_i4_e32 v91, v11, v71
	v_dot8c_i32_i4_e32 v90, v12, v76
	v_dot8c_i32_i4_e32 v91, v12, v72
	s_add_i32 s63, s57, -7
	v_dot8c_i32_i4_e32 v90, v13, v77
	v_dot8c_i32_i4_e32 v91, v13, v73
	s_bitcmp0_b32 s63, 6
	s_cselect_b64 vcc, -1, 0
	s_nop 0
	v_lshl_add_u32 v10, v90, 4, v91
	v_cvt_f32_i32_e32 v90, v10
	v_cndmask_b32_e32 v10, v79, v78, vcc
	s_nop 0
	v_readlane_b32 s63, v10, s63
	s_lshl_b32 s63, s63, 10
	s_add_i32 s63, s63, s62
	s_nop 2
	buffer_load_dwordx4 v[10:13], v0, s[92:95], s63 offen
	v_mov_b32_e32 v91, v1
	v_mov_b32_e32 v92, v1
	s_waitcnt vmcnt(5)
	v_dot8c_i32_i4_e32 v91, v26, v74
	v_dot8c_i32_i4_e32 v92, v26, v70
	v_dot8c_i32_i4_e32 v91, v27, v75
	v_dot8c_i32_i4_e32 v92, v27, v71
	v_dot8c_i32_i4_e32 v91, v28, v76
	v_dot8c_i32_i4_e32 v92, v28, v72
	s_add_i32 s63, s57, -6
	v_dot8c_i32_i4_e32 v91, v29, v77
	v_dot8c_i32_i4_e32 v92, v29, v73
	s_bitcmp0_b32 s63, 6
	s_cselect_b64 vcc, -1, 0
	s_nop 0
	v_lshl_add_u32 v26, v91, 4, v92
	v_cvt_f32_i32_e32 v91, v26
	v_cndmask_b32_e32 v26, v79, v78, vcc
	s_nop 0
	v_readlane_b32 s63, v26, s63
	s_lshl_b32 s63, s63, 10
	s_add_i32 s63, s63, s62
	s_nop 2
	buffer_load_dwordx4 v[26:29], v0, s[92:95], s63 offen
	v_mov_b32_e32 v92, v1
	v_mov_b32_e32 v93, v1
	s_waitcnt vmcnt(5)
	v_dot8c_i32_i4_e32 v92, v42, v74
	v_dot8c_i32_i4_e32 v93, v42, v70
	v_dot8c_i32_i4_e32 v92, v43, v75
	v_dot8c_i32_i4_e32 v93, v43, v71
	v_dot8c_i32_i4_e32 v92, v44, v76
	v_dot8c_i32_i4_e32 v93, v44, v72
	s_add_i32 s63, s57, -5
	v_dot8c_i32_i4_e32 v92, v45, v77
	v_dot8c_i32_i4_e32 v93, v45, v73
	s_bitcmp0_b32 s63, 6
	s_cselect_b64 vcc, -1, 0
	s_nop 0
	v_lshl_add_u32 v42, v92, 4, v93
	v_cvt_f32_i32_e32 v92, v42
	v_cndmask_b32_e32 v42, v79, v78, vcc
	s_nop 0
	v_readlane_b32 s63, v42, s63
	s_lshl_b32 s63, s63, 10
	s_add_i32 s63, s63, s62
	s_nop 2
	buffer_load_dwordx4 v[42:45], v0, s[92:95], s63 offen
	v_mov_b32_e32 v93, v1
	v_mov_b32_e32 v94, v1
	s_waitcnt vmcnt(5)
	v_dot8c_i32_i4_e32 v93, v58, v74
	v_dot8c_i32_i4_e32 v94, v58, v70
	v_dot8c_i32_i4_e32 v93, v59, v75
	v_dot8c_i32_i4_e32 v94, v59, v71
	v_dot8c_i32_i4_e32 v93, v60, v76
	v_dot8c_i32_i4_e32 v94, v60, v72
	s_add_i32 s63, s57, -4
	v_dot8c_i32_i4_e32 v93, v61, v77
	v_dot8c_i32_i4_e32 v94, v61, v73
	s_bitcmp0_b32 s63, 6
	s_cselect_b64 vcc, -1, 0
	s_nop 0
	v_lshl_add_u32 v58, v93, 4, v94
	v_cvt_f32_i32_e32 v93, v58
	v_cndmask_b32_e32 v58, v79, v78, vcc
	s_nop 0
	v_readlane_b32 s63, v58, s63
	s_lshl_b32 s63, s63, 10
	s_add_i32 s63, s63, s62
	s_nop 2
	buffer_load_dwordx4 v[58:61], v0, s[92:95], s63 offen
	v_mov_b32_e32 v94, v1
	v_mov_b32_e32 v95, v1
	s_waitcnt vmcnt(5)
	v_dot8c_i32_i4_e32 v94, v18, v74
	v_dot8c_i32_i4_e32 v95, v18, v70
	v_dot8c_i32_i4_e32 v94, v19, v75
	v_dot8c_i32_i4_e32 v95, v19, v71
	v_dot8c_i32_i4_e32 v94, v20, v76
	v_dot8c_i32_i4_e32 v95, v20, v72
	s_add_i32 s63, s57, -3
	v_dot8c_i32_i4_e32 v94, v21, v77
	v_dot8c_i32_i4_e32 v95, v21, v73
	s_bitcmp0_b32 s63, 6
	s_cselect_b64 vcc, -1, 0
	s_nop 0
	v_lshl_add_u32 v18, v94, 4, v95
	v_cvt_f32_i32_e32 v94, v18
	v_cndmask_b32_e32 v18, v79, v78, vcc
	s_nop 0
	v_readlane_b32 s63, v18, s63
	s_lshl_b32 s63, s63, 10
	s_add_i32 s63, s63, s62
	s_nop 2
	buffer_load_dwordx4 v[18:21], v0, s[92:95], s63 offen
	v_mov_b32_e32 v95, v1
	v_mov_b32_e32 v96, v1
	s_waitcnt vmcnt(5)
	v_dot8c_i32_i4_e32 v95, v34, v74
	v_dot8c_i32_i4_e32 v96, v34, v70
	v_dot8c_i32_i4_e32 v95, v35, v75
	v_dot8c_i32_i4_e32 v96, v35, v71
	v_dot8c_i32_i4_e32 v95, v36, v76
	v_dot8c_i32_i4_e32 v96, v36, v72
	s_add_i32 s63, s57, -2
	v_dot8c_i32_i4_e32 v95, v37, v77
	v_dot8c_i32_i4_e32 v96, v37, v73
	s_bitcmp0_b32 s63, 6
	s_cselect_b64 vcc, -1, 0
	s_nop 0
	v_lshl_add_u32 v34, v95, 4, v96
	v_cvt_f32_i32_e32 v95, v34
	v_cndmask_b32_e32 v34, v79, v78, vcc
	s_nop 0
	v_readlane_b32 s63, v34, s63
	s_lshl_b32 s63, s63, 10
	s_add_i32 s63, s63, s62
	s_nop 2
	buffer_load_dwordx4 v[34:37], v0, s[92:95], s63 offen
	v_mov_b32_e32 v96, v1
	v_mov_b32_e32 v97, v1
	s_waitcnt vmcnt(5)
	v_dot8c_i32_i4_e32 v96, v50, v74
	v_dot8c_i32_i4_e32 v97, v50, v70
	v_dot8c_i32_i4_e32 v96, v51, v75
	v_dot8c_i32_i4_e32 v97, v51, v71
	v_dot8c_i32_i4_e32 v96, v52, v76
	v_dot8c_i32_i4_e32 v97, v52, v72
	s_add_i32 s63, s57, -1
	v_dot8c_i32_i4_e32 v96, v53, v77
	v_dot8c_i32_i4_e32 v97, v53, v73
	s_bitcmp0_b32 s63, 6
	s_cselect_b64 vcc, -1, 0
	s_nop 0
	v_lshl_add_u32 v50, v96, 4, v97
	v_cvt_f32_i32_e32 v96, v50
	v_cndmask_b32_e32 v50, v79, v78, vcc
	s_nop 0
	v_readlane_b32 s63, v50, s63
	s_lshl_b32 s63, s63, 10
	s_add_i32 s63, s63, s62
	s_nop 2
	buffer_load_dwordx4 v[50:53], v0, s[92:95], s63 offen
	v_mov_b32_e32 v97, v1
	v_mov_b32_e32 v98, v1
	s_waitcnt vmcnt(5)
	v_dot8c_i32_i4_e32 v97, v62, v74
	v_dot8c_i32_i4_e32 v98, v62, v70
	v_dot8c_i32_i4_e32 v97, v63, v75
	v_dot8c_i32_i4_e32 v98, v63, v71
	v_dot8c_i32_i4_e32 v97, v64, v76
	v_dot8c_i32_i4_e32 v98, v64, v72
	v_dot8c_i32_i4_e32 v97, v65, v77
	v_dot8c_i32_i4_e32 v98, v65, v73
	s_bitcmp0_b32 s57, 6
	s_cselect_b64 vcc, -1, 0
	s_nop 0
	v_lshl_add_u32 v62, v97, 4, v98
	v_cvt_f32_i32_e32 v97, v62
	v_cndmask_b32_e32 v62, v79, v78, vcc
	s_nop 0
	v_readlane_b32 s63, v62, s57
	s_lshl_b32 s63, s63, 10
	s_add_i32 s63, s63, s62
	s_nop 2
	buffer_load_dwordx4 v[62:65], v0, s[92:95], s63 offen
	v_cndmask_b32_e64 v98, v90, v69, s[0:1]
	v_cndmask_b32_e64 v69, v69, v90, s[0:1]
	v_cndmask_b32_e64 v90, v91, v83, s[0:1]
	v_cndmask_b32_e64 v83, v83, v91, s[0:1]
	v_cndmask_b32_e64 v91, v92, v84, s[0:1]
	v_cndmask_b32_e64 v84, v84, v92, s[0:1]
	v_cndmask_b32_e64 v92, v93, v85, s[0:1]
	v_cndmask_b32_e64 v85, v85, v93, s[0:1]
	v_cndmask_b32_e64 v93, v94, v86, s[0:1]
	v_cndmask_b32_e64 v86, v86, v94, s[0:1]
	v_cndmask_b32_e64 v94, v95, v87, s[0:1]
	v_cndmask_b32_e64 v87, v87, v95, s[0:1]
	v_cndmask_b32_e64 v95, v96, v88, s[0:1]
	v_cndmask_b32_e64 v88, v88, v96, s[0:1]
	v_cndmask_b32_e64 v96, v97, v89, s[0:1]
	v_cndmask_b32_e64 v89, v89, v97, s[0:1]
	ds_bpermute_b32 v69, v190, v69
	ds_bpermute_b32 v83, v190, v83
	ds_bpermute_b32 v84, v190, v84
	ds_bpermute_b32 v85, v190, v85
	ds_bpermute_b32 v86, v190, v86
	ds_bpermute_b32 v87, v190, v87
	ds_bpermute_b32 v88, v190, v88
	ds_bpermute_b32 v89, v190, v89
	s_waitcnt lgkmcnt(7)
; __device__ __forceinline__ int shl_i(int v, int from_lane) { return __builtin_amdgcn_ds_bpermute(from_lane << 2, v); }
;     ...
;         const float wm = wave_max(fmaxf(fabsf(w0), fabsf(w1)));
;         const float wsq = (wm > 0.f) ? 127.0f / wm : 0.f;
;         const int q0 = (int)rintf(w0 * wsq), q1 = (int)rintf(w1 * wsq);
;         const int c8 = 8 * (int)wave_sum((float)(q0 + q1));
;         const int pk0 = (q0 & 0xFF) | ((shl_i(q0, lane + 1) & 0xFF) << 8) | ((shl_i(q0, lane + 2) & 0xFF) << 16) | (shl_i(q0, lane + 3) << 24);
;         const int pk1 = (q1 & 0xFF) | ((shl_i(q1, lane + 1) & 0xFF) << 8) | ((shl_i(q1, lane + 2) & 0xFF) << 16) | (shl_i(q1, lane + 3) << 24);
;         int acci[32];
; #pragma unroll
;         for (int i = 0; i < 32; ++i) acci[i] = 0;
	v_add_f32_e32 v69, v98, v69
	s_waitcnt lgkmcnt(6)
	v_add_f32_e32 v83, v90, v83
	s_waitcnt lgkmcnt(5)
	v_add_f32_e32 v84, v91, v84
	s_waitcnt lgkmcnt(4)
	v_add_f32_e32 v85, v92, v85
	s_waitcnt lgkmcnt(3)
	v_add_f32_e32 v86, v93, v86
	s_waitcnt lgkmcnt(2)
	v_add_f32_e32 v87, v94, v87
	s_waitcnt lgkmcnt(1)
	v_add_f32_e32 v88, v95, v88
	s_waitcnt lgkmcnt(0)
	v_add_f32_e32 v89, v96, v89
	v_cndmask_b32_e64 v90, v86, v69, s[2:3]
	v_cndmask_b32_e64 v69, v69, v86, s[2:3]
	v_cndmask_b32_e64 v86, v87, v83, s[2:3]
	v_cndmask_b32_e64 v83, v83, v87, s[2:3]
	v_cndmask_b32_e64 v87, v88, v84, s[2:3]
	v_cndmask_b32_e64 v84, v84, v88, s[2:3]
	v_cndmask_b32_e64 v88, v89, v85, s[2:3]
	v_cndmask_b32_e64 v85, v85, v89, s[2:3]
	ds_bpermute_b32 v69, v189, v69
	ds_bpermute_b32 v83, v189, v83
	ds_bpermute_b32 v84, v189, v84
	ds_bpermute_b32 v85, v189, v85
	s_add_i32 s57, s57, 16
	s_waitcnt lgkmcnt(3)
	v_add_f32_e32 v69, v90, v69
	s_waitcnt lgkmcnt(2)
	v_add_f32_e32 v83, v86, v83
	s_waitcnt lgkmcnt(1)
	v_add_f32_e32 v84, v87, v84
	s_waitcnt lgkmcnt(0)
	v_add_f32_e32 v85, v88, v85
	v_cndmask_b32_e64 v86, v84, v69, s[4:5]
	v_cndmask_b32_e64 v69, v69, v84, s[4:5]
	v_cndmask_b32_e64 v84, v85, v83, s[4:5]
	v_cndmask_b32_e64 v83, v83, v85, s[4:5]
	ds_bpermute_b32 v69, v188, v69
	ds_bpermute_b32 v83, v188, v83
	s_waitcnt lgkmcnt(1)
	v_add_f32_e32 v69, v86, v69
	s_waitcnt lgkmcnt(0)
	v_add_f32_e32 v83, v84, v83
	v_cndmask_b32_e64 v84, v83, v69, s[6:7]
	v_cndmask_b32_e64 v69, v69, v83, s[6:7]
	ds_bpermute_b32 v69, v163, v69
	s_waitcnt lgkmcnt(0)
	v_add_f32_e32 v69, v84, v69
	v_mov_b32_e32 v83, v69
	s_nop 1
	v_permlane16_swap_b32_e32 v69, v83
	v_add_f32_e32 v69, v69, v83
	v_mov_b32_e32 v83, v69
	s_nop 1
	v_permlane32_swap_b32_e32 v69, v83
	v_add_f32_e32 v69, v69, v83
	v_mul_f32_e32 v69, v66, v69
	v_fma_f32 v83, |v69|, s66, 1.0
	v_rcp_f32_e32 v83, v83
	v_mul_f32_e32 v84, v69, v69
	v_mul_f32_e32 v84, 0xbf38aa3b, v84
	v_exp_f32_e32 v84, v84
	v_fmamk_f32 v85, v83, 0x3f07dc22, v207
	v_fmaak_f32 v85, v83, v85, 0x3f35f0e3
	v_fmaak_f32 v85, v83, v85, 0xbe11a98e
	v_fmaak_f32 v85, v83, v85, 0x3e027906
	v_mul_f32_e32 v83, v83, v85
	v_mul_f32_e32 v83, v84, v83
	v_mul_f32_e32 v84, v69, v83
	v_fma_f32 v83, -v69, v83, v69
	v_cmp_gt_f32_e32 vcc, 0, v69
	s_nop 1
	v_cndmask_b32_e32 v69, v83, v84, vcc
	v_mul_f32_e32 v69, 0x3d4ccccd, v69
	v_mul_f32_e32 v69, v80, v69
	v_cmp_eq_u32_e32 vcc, s56, v193
	s_add_i32 s56, s56, 1
	s_cmpk_eq_i32 s57, 0x9f
	v_cndmask_b32_e32 v82, v82, v69, vcc
	s_cbranch_scc0 .LBB0_1421
	v_max_f32_e64 v66, |v82|, |v82|
	v_max_f32_e64 v69, |v81|, |v81|
	v_max_f32_e32 v66, v69, v66
	v_mov_b32_e32 v69, 0
	s_mov_b32 s57, 0x42fe0000
	v_mbcnt_lo_u32_b32 v69, -1, v69
	v_mbcnt_hi_u32_b32 v69, -1, v69
	v_lshlrev_b32_e32 v71, 2, v69
	v_xor_b32_e32 v69, 0x80, v71
	ds_bpermute_b32 v69, v69, v66
	v_xor_b32_e32 v70, 64, v71
	v_xor_b32_e32 v72, 8, v71
	v_mov_b32_e32 v83, 0
	s_waitcnt lgkmcnt(0)
	v_max_f32_e32 v69, v69, v69
	v_max_f32_e32 v66, v66, v69
	ds_bpermute_b32 v69, v70, v66
	v_xor_b32_e32 v70, 32, v71
	s_movk_i32 s56, 0x9f
	v_mov_b32_e32 v74, 0
	v_mov_b32_e32 v75, 0
	s_waitcnt lgkmcnt(0)
	v_max_f32_e32 v69, v69, v69
	v_max_f32_e32 v66, v66, v69
	ds_bpermute_b32 v69, v70, v66
	v_xor_b32_e32 v70, 16, v71
	v_xor_b32_e32 v71, 4, v71
	v_mov_b32_e32 v76, 0
	v_mov_b32_e32 v80, 0
	s_waitcnt lgkmcnt(0)
	v_max_f32_e32 v69, v69, v69
	v_max_f32_e32 v69, v66, v69
	ds_bpermute_b32 v70, v70, v69
	v_mov_b32_e32 v66, 0
	v_mov_b32_e32 v94, 0
	v_mov_b32_e32 v95, 0
	v_mov_b32_e32 v96, 0
	s_waitcnt lgkmcnt(0)
	v_max_f32_e32 v70, v70, v70
	v_max_f32_e32 v73, v69, v70
	ds_bpermute_b32 v72, v72, v73
	v_mov_b32_e32 v69, 0
	v_mov_b32_e32 v70, 0
	v_mov_b32_e32 v97, 0
	v_mov_b32_e32 v98, 0
	s_waitcnt lgkmcnt(0)
	v_max_f32_e32 v72, v72, v72
	v_max_f32_e32 v77, v73, v72
	ds_bpermute_b32 v71, v71, v77
	v_mov_b32_e32 v72, 0
	v_mov_b32_e32 v73, 0
	v_mov_b32_e32 v99, 0
	v_mov_b32_e32 v100, 0
	s_waitcnt lgkmcnt(0)
	v_max_f32_e32 v71, v71, v71
	v_max_f32_e32 v71, v77, v71
	v_div_scale_f32 v77, s[62:63], v71, v71, s57
	v_rcp_f32_e32 v84, v77
	v_div_scale_f32 v85, vcc, s57, v71, s57
	v_mov_b32_e32 v101, 0
	v_fma_f32 v86, -v77, v84, 1.0
	v_fmac_f32_e32 v84, v86, v84
	v_mul_f32_e32 v86, v85, v84
	v_fma_f32 v87, -v77, v86, v85
	v_fmac_f32_e32 v86, v87, v84
	v_fma_f32 v77, -v77, v86, v85
	v_div_fmas_f32 v77, v77, v84, v86
	v_div_fixup_f32 v77, v77, v71, s57
	v_cmp_lt_f32_e32 vcc, 0, v71
	s_mov_b32 s57, 0xc0c0500
	v_mov_b32_e32 v85, 0
	v_cndmask_b32_e32 v77, 0, v77, vcc
	v_mul_f32_e32 v81, v81, v77
	v_mul_f32_e32 v77, v82, v77
	v_rndne_f32_e32 v81, v81
	v_rndne_f32_e32 v77, v77
	v_cvt_i32_f32_e32 v82, v81
	v_cvt_i32_f32_e32 v107, v77
	v_mbcnt_lo_u32_b32 v81, -1, v83
	v_mbcnt_hi_u32_b32 v81, -1, v81
	v_lshlrev_b32_e32 v84, 2, v81
	v_add_u32_e32 v83, v82, v107
	v_cvt_f32_i32_e32 v83, v83
	v_xor_b32_e32 v81, 0x80, v84
	v_xor_b32_e32 v88, 64, v84
	v_xor_b32_e32 v89, 16, v84
	ds_bpermute_b32 v87, v81, v83
	v_xor_b32_e32 v90, 8, v84
	ds_bpermute_b32 v91, v195, v82
	ds_bpermute_b32 v92, v196, v82
	ds_bpermute_b32 v108, v194, v107
	s_waitcnt lgkmcnt(3)
	v_add_f32_e32 v83, v87, v83
	ds_bpermute_b32 v87, v88, v83
	v_xor_b32_e32 v88, 32, v84
	v_xor_b32_e32 v84, 4, v84
	ds_bpermute_b32 v109, v195, v107
	ds_bpermute_b32 v110, v196, v107
	s_waitcnt lgkmcnt(2)
	v_add_f32_e32 v83, v83, v87
	ds_bpermute_b32 v87, v88, v83
	ds_bpermute_b32 v88, v194, v82
	v_mov_b32_e32 v77, 0
	v_mov_b32_e32 v81, 0
	v_mov_b32_e32 v86, 0
	s_waitcnt lgkmcnt(1)
	v_add_f32_e32 v83, v83, v87
	ds_bpermute_b32 v87, v89, v83
	s_waitcnt lgkmcnt(1)
	v_lshlrev_b32_e32 v88, 8, v88
	v_lshlrev_b32_e32 v89, 16, v91
	v_perm_b32 v82, v88, v82, s57
	v_and_b32_e32 v88, 0xff0000, v89
	s_waitcnt lgkmcnt(0)
	v_add_f32_e32 v83, v83, v87
	ds_bpermute_b32 v87, v90, v83
	v_lshlrev_b32_e32 v90, 24, v92
	v_or3_b32 v111, v82, v88, v90
	v_mov_b32_e32 v82, 0
	v_mov_b32_e32 v88, 0
	s_waitcnt lgkmcnt(0)
	v_add_f32_e32 v103, v83, v87
	ds_bpermute_b32 v104, v84, v103
	v_mov_b32_e32 v84, 0
	v_mov_b32_e32 v87, 0
	v_mov_b32_e32 v89, 0
	v_mov_b32_e32 v90, 0
	v_mov_b32_e32 v91, 0
	v_mov_b32_e32 v92, 0
	v_mov_b32_e32 v93, 0
	v_mov_b32_e32 v102, 0
	v_mov_b32_e32 v83, 0
	s_cmp_eq_u32 s101, 0
	s_cbranch_scc1 .Lnb_1423
	s_barrier
